# all four GEMM K-loops: lgkmcnt(0) at MFMA-phase head replaced by counted lgkmcnt waits at each fragment's first consumer MFMA
# speedup vs baseline: 1.0018x; 1.0018x over previous
.LBB3_34:
	s_add_u32 s26, s20, s24
	s_addc_u32 s27, s21, s25
	s_add_u32 s26, s26, 0x180
	s_addc_u32 s27, s27, 0
	s_add_u32 s64, s22, s24
	s_addc_u32 s65, s23, s25
	s_add_u32 s66, s64, 0x180
	s_addc_u32 s67, s65, 0
	s_cmp_eq_u32 s56, s63
	s_cselect_b32 s65, s5, s27
	s_cselect_b32 s64, s4, s26
	s_cselect_b32 s27, s7, s67
	s_cselect_b32 s26, s6, s66
	s_add_i32 s66, s58, s38
	v_lshl_add_u64 v[146:147], v[72:73], 0, s[24:25]
	s_mov_b32 m0, s66
	ds_read_b128 v[98:101], v94 offset:16384
	ds_read_b128 v[102:105], v94 offset:17408
	ds_read_b128 v[106:109], v94 offset:18432
	ds_read_b128 v[110:113], v94 offset:19456
	ds_read_b128 v[114:117], v95
	ds_read_b128 v[118:121], v95 offset:1024
	ds_read_b128 v[122:125], v95 offset:2048
	ds_read_b128 v[126:129], v95 offset:3072
	ds_read_b128 v[130:133], v95 offset:4096
	ds_read_b128 v[134:137], v95 offset:5120
	ds_read_b128 v[138:141], v95 offset:6144
	ds_read_b128 v[142:145], v95 offset:7168
	global_load_lds_dwordx4 v[146:147], off
	v_lshl_add_u64 v[146:147], v[74:75], 0, s[24:25]
	s_add_i32 m0, s66, 0x2000
	s_nop 0
	global_load_lds_dwordx4 v[146:147], off
	s_barrier
	s_setprio 1
	s_waitcnt lgkmcnt(7)
	v_mfma_f32_16x16x32_f16 v[44:47], v[98:101], v[114:117], v[44:47]
	v_mfma_f32_16x16x32_f16 v[40:43], v[106:109], v[114:117], v[40:43]
	s_waitcnt lgkmcnt(5)
	v_mfma_f32_16x16x32_f16 v[32:35], v[98:101], v[122:125], v[32:35]
	v_mfma_f32_16x16x32_f16 v[28:31], v[106:109], v[122:125], v[28:31]
	s_waitcnt lgkmcnt(3)
	v_mfma_f32_16x16x32_f16 v[20:23], v[98:101], v[130:133], v[20:23]
	v_mfma_f32_16x16x32_f16 v[16:19], v[106:109], v[130:133], v[16:19]
	s_waitcnt lgkmcnt(1)
	v_mfma_f32_16x16x32_f16 v[8:11], v[98:101], v[138:141], v[8:11]
	v_mfma_f32_16x16x32_f16 v[4:7], v[106:109], v[138:141], v[4:7]
	v_mfma_f32_16x16x32_f16 v[44:47], v[102:105], v[118:121], v[44:47]
	v_mfma_f32_16x16x32_f16 v[40:43], v[110:113], v[118:121], v[40:43]
	v_mfma_f32_16x16x32_f16 v[32:35], v[102:105], v[126:129], v[32:35]
	v_mfma_f32_16x16x32_f16 v[28:31], v[110:113], v[126:129], v[28:31]
	v_mfma_f32_16x16x32_f16 v[20:23], v[102:105], v[134:137], v[20:23]
	v_mfma_f32_16x16x32_f16 v[16:19], v[110:113], v[134:137], v[16:19]
	s_waitcnt lgkmcnt(0)
	v_mfma_f32_16x16x32_f16 v[8:11], v[102:105], v[142:145], v[8:11]
	v_mfma_f32_16x16x32_f16 v[4:7], v[110:113], v[142:145], v[4:7]
	s_setprio 0
	s_barrier
	v_lshl_add_u64 v[106:107], v[76:77], 0, s[24:25]
	s_add_i32 m0, s43, 0x18000
	ds_read_b128 v[98:101], v94 offset:20480
	ds_read_b128 v[102:105], v94 offset:21504
	global_load_lds_dwordx4 v[106:107], off
	v_lshl_add_u64 v[106:107], v[78:79], 0, s[24:25]
	s_add_i32 m0, s43, 0x1a000
	s_nop 0
	global_load_lds_dwordx4 v[106:107], off
	v_lshl_add_u64 v[106:107], v[80:81], 0, s[24:25]
	s_add_i32 m0, s43, 0x1c000
	s_nop 0
	global_load_lds_dwordx4 v[106:107], off
	s_waitcnt vmcnt(5)
	s_barrier
	s_setprio 1
	s_waitcnt lgkmcnt(1)
	v_mfma_f32_16x16x32_f16 v[36:39], v[98:101], v[114:117], v[36:39]
	v_mfma_f32_16x16x32_f16 v[24:27], v[98:101], v[122:125], v[24:27]
	v_mfma_f32_16x16x32_f16 v[12:15], v[98:101], v[130:133], v[12:15]
	v_mfma_f32_16x16x32_f16 v[0:3], v[98:101], v[138:141], v[0:3]
	s_waitcnt lgkmcnt(0)
	v_mfma_f32_16x16x32_f16 v[36:39], v[102:105], v[118:121], v[36:39]
	v_mfma_f32_16x16x32_f16 v[24:27], v[102:105], v[126:129], v[24:27]
	v_mfma_f32_16x16x32_f16 v[12:15], v[102:105], v[134:137], v[12:15]
	v_mfma_f32_16x16x32_f16 v[0:3], v[102:105], v[142:145], v[0:3]
	s_setprio 0
	s_barrier
	s_mov_b32 m0, s43
	v_lshl_add_u64 v[146:147], s[64:65], 0, v[48:49]
	ds_read_b128 v[98:101], v94 offset:57344
	ds_read_b128 v[102:105], v94 offset:58368
	ds_read_b128 v[106:109], v94 offset:59392
	ds_read_b128 v[110:113], v94 offset:60416
	ds_read_b128 v[114:117], v95 offset:40960
	ds_read_b128 v[118:121], v95 offset:41984
	ds_read_b128 v[122:125], v95 offset:43008
	ds_read_b128 v[126:129], v95 offset:44032
	ds_read_b128 v[130:133], v95 offset:45056
	ds_read_b128 v[134:137], v95 offset:46080
	ds_read_b128 v[138:141], v95 offset:47104
	ds_read_b128 v[142:145], v95 offset:48128
	global_load_lds_dwordx4 v[146:147], off
	v_lshl_add_u64 v[148:149], s[64:65], 0, v[52:53]
	s_mov_b32 m0, s44
	s_nop 0
	global_load_lds_dwordx4 v[148:149], off
	s_barrier
	s_setprio 1
	s_waitcnt lgkmcnt(7)
	v_mfma_f32_16x16x32_f16 v[44:47], v[98:101], v[114:117], v[44:47]
	v_mfma_f32_16x16x32_f16 v[40:43], v[106:109], v[114:117], v[40:43]
	s_waitcnt lgkmcnt(5)
	v_mfma_f32_16x16x32_f16 v[32:35], v[98:101], v[122:125], v[32:35]
	v_mfma_f32_16x16x32_f16 v[28:31], v[106:109], v[122:125], v[28:31]
	s_waitcnt lgkmcnt(3)
	v_mfma_f32_16x16x32_f16 v[20:23], v[98:101], v[130:133], v[20:23]
	v_mfma_f32_16x16x32_f16 v[16:19], v[106:109], v[130:133], v[16:19]
	s_waitcnt lgkmcnt(1)
	v_mfma_f32_16x16x32_f16 v[8:11], v[98:101], v[138:141], v[8:11]
	v_mfma_f32_16x16x32_f16 v[4:7], v[106:109], v[138:141], v[4:7]
	v_mfma_f32_16x16x32_f16 v[44:47], v[102:105], v[118:121], v[44:47]
	v_mfma_f32_16x16x32_f16 v[40:43], v[110:113], v[118:121], v[40:43]
	v_mfma_f32_16x16x32_f16 v[32:35], v[102:105], v[126:129], v[32:35]
	v_mfma_f32_16x16x32_f16 v[28:31], v[110:113], v[126:129], v[28:31]
	v_mfma_f32_16x16x32_f16 v[20:23], v[102:105], v[134:137], v[20:23]
	v_mfma_f32_16x16x32_f16 v[16:19], v[110:113], v[134:137], v[16:19]
	s_waitcnt lgkmcnt(0)
	v_mfma_f32_16x16x32_f16 v[8:11], v[102:105], v[142:145], v[8:11]
	v_mfma_f32_16x16x32_f16 v[4:7], v[110:113], v[142:145], v[4:7]
	s_setprio 0
	s_barrier
	s_mov_b32 m0, s45
	v_lshl_add_u64 v[150:151], s[26:27], 0, v[50:51]
	ds_read_b128 v[98:101], v94 offset:61440
	ds_read_b128 v[102:105], v94 offset:62464
	global_load_lds_dwordx4 v[150:151], off
	v_lshl_add_u64 v[152:153], s[26:27], 0, v[54:55]
	s_mov_b32 m0, s46
	v_lshl_add_u64 v[154:155], s[26:27], 0, v[56:57]
	global_load_lds_dwordx4 v[152:153], off
	s_mov_b32 m0, s47
	s_nop 0
	global_load_lds_dwordx4 v[154:155], off
	s_waitcnt vmcnt(5)
	s_barrier
	s_setprio 1
	s_waitcnt lgkmcnt(1)
	v_mfma_f32_16x16x32_f16 v[36:39], v[98:101], v[114:117], v[36:39]
	v_mfma_f32_16x16x32_f16 v[24:27], v[98:101], v[122:125], v[24:27]
	v_mfma_f32_16x16x32_f16 v[12:15], v[98:101], v[130:133], v[12:15]
	v_mfma_f32_16x16x32_f16 v[0:3], v[98:101], v[138:141], v[0:3]
	s_waitcnt lgkmcnt(0)
	v_mfma_f32_16x16x32_f16 v[36:39], v[102:105], v[118:121], v[36:39]
	v_mfma_f32_16x16x32_f16 v[24:27], v[102:105], v[126:129], v[24:27]
	v_mfma_f32_16x16x32_f16 v[12:15], v[102:105], v[134:137], v[12:15]
	v_mfma_f32_16x16x32_f16 v[0:3], v[102:105], v[142:145], v[0:3]
	s_setprio 0
	s_barrier
	s_mov_b32 m0, s52
	v_lshl_add_u64 v[146:147], v[146:147], 0, s[16:17]
	ds_read_b128 v[98:101], v96
	ds_read_b128 v[102:105], v96 offset:1024
	ds_read_b128 v[106:109], v96 offset:2048
	ds_read_b128 v[110:113], v96 offset:3072
	ds_read_b128 v[114:117], v97
	ds_read_b128 v[118:121], v97 offset:1024
	ds_read_b128 v[122:125], v97 offset:2048
	ds_read_b128 v[126:129], v97 offset:3072
	ds_read_b128 v[130:133], v97 offset:4096
	ds_read_b128 v[134:137], v97 offset:5120
	ds_read_b128 v[138:141], v97 offset:6144
	ds_read_b128 v[142:145], v97 offset:7168
	global_load_lds_dwordx4 v[146:147], off
	v_lshl_add_u64 v[146:147], v[148:149], 0, s[16:17]
	s_mov_b32 m0, s53
	s_nop 0
	global_load_lds_dwordx4 v[146:147], off
	s_barrier
	s_setprio 1
	s_waitcnt lgkmcnt(7)
	v_mfma_f32_16x16x32_f16 v[44:47], v[98:101], v[114:117], v[44:47]
	v_mfma_f32_16x16x32_f16 v[40:43], v[106:109], v[114:117], v[40:43]
	s_waitcnt lgkmcnt(5)
	v_mfma_f32_16x16x32_f16 v[32:35], v[98:101], v[122:125], v[32:35]
	v_mfma_f32_16x16x32_f16 v[28:31], v[106:109], v[122:125], v[28:31]
	s_waitcnt lgkmcnt(3)
	v_mfma_f32_16x16x32_f16 v[20:23], v[98:101], v[130:133], v[20:23]
	v_mfma_f32_16x16x32_f16 v[16:19], v[106:109], v[130:133], v[16:19]
	s_waitcnt lgkmcnt(1)
	v_mfma_f32_16x16x32_f16 v[8:11], v[98:101], v[138:141], v[8:11]
	v_mfma_f32_16x16x32_f16 v[4:7], v[106:109], v[138:141], v[4:7]
	v_mfma_f32_16x16x32_f16 v[44:47], v[102:105], v[118:121], v[44:47]
	v_mfma_f32_16x16x32_f16 v[40:43], v[110:113], v[118:121], v[40:43]
	v_mfma_f32_16x16x32_f16 v[32:35], v[102:105], v[126:129], v[32:35]
	v_mfma_f32_16x16x32_f16 v[28:31], v[110:113], v[126:129], v[28:31]
	v_mfma_f32_16x16x32_f16 v[20:23], v[102:105], v[134:137], v[20:23]
	v_mfma_f32_16x16x32_f16 v[16:19], v[110:113], v[134:137], v[16:19]
	s_waitcnt lgkmcnt(0)
	v_mfma_f32_16x16x32_f16 v[8:11], v[102:105], v[142:145], v[8:11]
	v_mfma_f32_16x16x32_f16 v[4:7], v[110:113], v[142:145], v[4:7]
	s_setprio 0
	s_barrier
	s_mov_b32 m0, s54
	v_lshl_add_u64 v[106:107], v[150:151], 0, s[16:17]
	ds_read_b128 v[98:101], v96 offset:4096
	ds_read_b128 v[102:105], v96 offset:5120
	global_load_lds_dwordx4 v[106:107], off
	v_lshl_add_u64 v[106:107], v[152:153], 0, s[16:17]
	s_add_i32 m0, s54, 0x2000
	s_nop 0
	global_load_lds_dwordx4 v[106:107], off
	v_lshl_add_u64 v[106:107], v[154:155], 0, s[16:17]
	s_add_i32 m0, s54, 0x4000
	s_nop 0
	global_load_lds_dwordx4 v[106:107], off
	s_waitcnt vmcnt(5)
	s_barrier
	s_setprio 1
	s_waitcnt lgkmcnt(1)
	v_mfma_f32_16x16x32_f16 v[36:39], v[98:101], v[114:117], v[36:39]
	v_mfma_f32_16x16x32_f16 v[24:27], v[98:101], v[122:125], v[24:27]
	v_mfma_f32_16x16x32_f16 v[12:15], v[98:101], v[130:133], v[12:15]
	v_mfma_f32_16x16x32_f16 v[0:3], v[98:101], v[138:141], v[0:3]
	s_waitcnt lgkmcnt(0)
	v_mfma_f32_16x16x32_f16 v[36:39], v[102:105], v[118:121], v[36:39]
	v_mfma_f32_16x16x32_f16 v[24:27], v[102:105], v[126:129], v[24:27]
	v_mfma_f32_16x16x32_f16 v[12:15], v[102:105], v[134:137], v[12:15]
	v_mfma_f32_16x16x32_f16 v[0:3], v[102:105], v[142:145], v[0:3]
	s_setprio 0
	s_barrier
	s_add_i32 s63, s63, 3
	s_add_u32 s24, s24, 0x180
	s_addc_u32 s25, s25, 0
	s_cmp_ge_i32 s63, s49
	s_cbranch_scc0 .LBB3_34
	s_branch .LBB3_21

.LBB4_22:
	s_add_u32 s34, s26, s30
	s_addc_u32 s35, s27, s31
	s_add_u32 s34, s34, 0x180
	s_addc_u32 s35, s35, 0
	s_add_u32 s68, s28, s30
	s_addc_u32 s69, s29, s31
	s_add_u32 s70, s68, 0x180
	s_addc_u32 s71, s69, 0
	s_cmp_eq_u32 s60, s67
	s_cselect_b32 s69, s5, s35
	s_cselect_b32 s68, s4, s34
	s_cselect_b32 s35, s7, s71
	s_cselect_b32 s34, s6, s70
	s_add_i32 s70, s62, s44
	v_lshl_add_u64 v[108:109], v[98:99], 0, s[30:31]
	s_mov_b32 m0, s70
	ds_read_b128 v[130:133], v136 offset:16384
	ds_read_b128 v[142:145], v136 offset:17408
	ds_read_b128 v[146:149], v136 offset:18432
	ds_read_b128 v[150:153], v136 offset:19456
	ds_read_b128 v[154:157], v137
	ds_read_b128 v[158:161], v137 offset:1024
	ds_read_b128 v[162:165], v137 offset:2048
	ds_read_b128 v[166:169], v137 offset:3072
	ds_read_b128 v[170:173], v137 offset:4096
	ds_read_b128 v[174:177], v137 offset:5120
	ds_read_b128 v[178:181], v137 offset:6144
	ds_read_b128 v[182:185], v137 offset:7168
	global_load_lds_dwordx4 v[108:109], off
	v_lshl_add_u64 v[108:109], v[100:101], 0, s[30:31]
	s_add_i32 m0, s70, 0x2000
	s_nop 0
	global_load_lds_dwordx4 v[108:109], off
	s_barrier
	s_setprio 1
	s_waitcnt lgkmcnt(7)
	v_mfma_f32_16x16x32_f16 v[94:97], v[130:133], v[154:157], v[94:97]
	v_mfma_f32_16x16x32_f16 v[90:93], v[146:149], v[154:157], v[90:93]
	s_waitcnt lgkmcnt(5)
	v_mfma_f32_16x16x32_f16 v[82:85], v[130:133], v[162:165], v[82:85]
	v_mfma_f32_16x16x32_f16 v[78:81], v[146:149], v[162:165], v[78:81]
	s_waitcnt lgkmcnt(3)
	v_mfma_f32_16x16x32_f16 v[70:73], v[130:133], v[170:173], v[70:73]
	v_mfma_f32_16x16x32_f16 v[66:69], v[146:149], v[170:173], v[66:69]
	s_waitcnt lgkmcnt(1)
	v_mfma_f32_16x16x32_f16 v[58:61], v[130:133], v[178:181], v[58:61]
	v_mfma_f32_16x16x32_f16 v[54:57], v[146:149], v[178:181], v[54:57]
	v_mfma_f32_16x16x32_f16 v[94:97], v[142:145], v[158:161], v[94:97]
	v_mfma_f32_16x16x32_f16 v[90:93], v[150:153], v[158:161], v[90:93]
	v_mfma_f32_16x16x32_f16 v[82:85], v[142:145], v[166:169], v[82:85]
	v_mfma_f32_16x16x32_f16 v[78:81], v[150:153], v[166:169], v[78:81]
	v_mfma_f32_16x16x32_f16 v[70:73], v[142:145], v[174:177], v[70:73]
	v_mfma_f32_16x16x32_f16 v[66:69], v[150:153], v[174:177], v[66:69]
	s_waitcnt lgkmcnt(0)
	v_mfma_f32_16x16x32_f16 v[58:61], v[142:145], v[182:185], v[58:61]
	v_mfma_f32_16x16x32_f16 v[54:57], v[150:153], v[182:185], v[54:57]
	s_setprio 0
	s_barrier
	v_lshl_add_u64 v[108:109], v[102:103], 0, s[30:31]
	s_add_i32 m0, s49, 0x18000
	ds_read_b128 v[130:133], v136 offset:20480
	ds_read_b128 v[142:145], v136 offset:21504
	global_load_lds_dwordx4 v[108:109], off
	v_lshl_add_u64 v[108:109], v[104:105], 0, s[30:31]
	s_add_i32 m0, s49, 0x1a000
	s_nop 0
	global_load_lds_dwordx4 v[108:109], off
	v_lshl_add_u64 v[108:109], v[106:107], 0, s[30:31]
	s_add_i32 m0, s49, 0x1c000
	s_nop 0
	global_load_lds_dwordx4 v[108:109], off
	s_cmp_lg_u32 s67, 0
	s_cbranch_scc1 .Lpj_norm_0
	s_mul_i32 s72, s66, 0xc0
	v_add_u32_e32 v214, s72, v135
	v_ashrrev_i32_e32 v215, 31, v214
	v_lshl_add_u64 v[214:215], v[214:215], 2, s[10:11]
	global_load_dwordx4 v[202:205], v[214:215], off
	global_load_dwordx4 v[206:209], v[214:215], off offset:64
	global_load_dwordx4 v[210:213], v[214:215], off offset:128
	global_load_dwordx4 v[2:5], v[194:195], off
	global_load_dwordx4 v[6:9], v[194:195], off offset:64
	global_load_dwordx4 v[10:13], v[194:195], off offset:128
	global_load_dwordx4 v[14:17], v[196:197], off
	s_waitcnt vmcnt(12)
	s_branch .Lpj_join_0

.Lpj_join_0:
	s_barrier
	s_setprio 1
	s_waitcnt lgkmcnt(1)
	v_mfma_f32_16x16x32_f16 v[86:89], v[130:133], v[154:157], v[86:89]
	v_mfma_f32_16x16x32_f16 v[74:77], v[130:133], v[162:165], v[74:77]
	v_mfma_f32_16x16x32_f16 v[62:65], v[130:133], v[170:173], v[62:65]
	v_mfma_f32_16x16x32_f16 v[50:53], v[130:133], v[178:181], v[50:53]
	s_waitcnt lgkmcnt(0)
	v_mfma_f32_16x16x32_f16 v[86:89], v[142:145], v[158:161], v[86:89]
	v_mfma_f32_16x16x32_f16 v[74:77], v[142:145], v[166:169], v[74:77]
	v_mfma_f32_16x16x32_f16 v[62:65], v[142:145], v[174:177], v[62:65]
	v_mfma_f32_16x16x32_f16 v[50:53], v[142:145], v[182:185], v[50:53]
	s_setprio 0
	s_barrier
	s_mov_b32 m0, s49
	v_lshl_add_u64 v[108:109], s[68:69], 0, v[110:111]
	ds_read_b128 v[130:133], v136 offset:57344
	ds_read_b128 v[142:145], v136 offset:58368
	ds_read_b128 v[146:149], v136 offset:59392
	ds_read_b128 v[150:153], v136 offset:60416
	ds_read_b128 v[154:157], v137 offset:40960
	ds_read_b128 v[158:161], v137 offset:41984
	ds_read_b128 v[162:165], v137 offset:43008
	ds_read_b128 v[166:169], v137 offset:44032
	ds_read_b128 v[170:173], v137 offset:45056
	ds_read_b128 v[174:177], v137 offset:46080
	ds_read_b128 v[178:181], v137 offset:47104
	ds_read_b128 v[182:185], v137 offset:48128
	global_load_lds_dwordx4 v[108:109], off
	v_lshl_add_u64 v[186:187], s[68:69], 0, v[114:115]
	s_mov_b32 m0, s50
	s_nop 0
	global_load_lds_dwordx4 v[186:187], off
	s_barrier
	s_setprio 1
	s_waitcnt lgkmcnt(7)
	v_mfma_f32_16x16x32_f16 v[94:97], v[130:133], v[154:157], v[94:97]
	v_mfma_f32_16x16x32_f16 v[90:93], v[146:149], v[154:157], v[90:93]
	s_waitcnt lgkmcnt(5)
	v_mfma_f32_16x16x32_f16 v[82:85], v[130:133], v[162:165], v[82:85]
	v_mfma_f32_16x16x32_f16 v[78:81], v[146:149], v[162:165], v[78:81]
	s_waitcnt lgkmcnt(3)
	v_mfma_f32_16x16x32_f16 v[70:73], v[130:133], v[170:173], v[70:73]
	v_mfma_f32_16x16x32_f16 v[66:69], v[146:149], v[170:173], v[66:69]
	s_waitcnt lgkmcnt(1)
	v_mfma_f32_16x16x32_f16 v[58:61], v[130:133], v[178:181], v[58:61]
	v_mfma_f32_16x16x32_f16 v[54:57], v[146:149], v[178:181], v[54:57]
	v_mfma_f32_16x16x32_f16 v[94:97], v[142:145], v[158:161], v[94:97]
	v_mfma_f32_16x16x32_f16 v[90:93], v[150:153], v[158:161], v[90:93]
	v_mfma_f32_16x16x32_f16 v[82:85], v[142:145], v[166:169], v[82:85]
	v_mfma_f32_16x16x32_f16 v[78:81], v[150:153], v[166:169], v[78:81]
	v_mfma_f32_16x16x32_f16 v[70:73], v[142:145], v[174:177], v[70:73]
	v_mfma_f32_16x16x32_f16 v[66:69], v[150:153], v[174:177], v[66:69]
	s_waitcnt lgkmcnt(0)
	v_mfma_f32_16x16x32_f16 v[58:61], v[142:145], v[182:185], v[58:61]
	v_mfma_f32_16x16x32_f16 v[54:57], v[150:153], v[182:185], v[54:57]
	s_setprio 0
	s_barrier
	s_mov_b32 m0, s51
	v_lshl_add_u64 v[188:189], s[34:35], 0, v[112:113]
	ds_read_b128 v[130:133], v136 offset:61440
	ds_read_b128 v[142:145], v136 offset:62464
	global_load_lds_dwordx4 v[188:189], off
	v_lshl_add_u64 v[190:191], s[34:35], 0, v[116:117]
	s_mov_b32 m0, s52
	v_lshl_add_u64 v[192:193], s[34:35], 0, v[118:119]
	global_load_lds_dwordx4 v[190:191], off
	s_mov_b32 m0, s53
	s_nop 0
	global_load_lds_dwordx4 v[192:193], off
	s_cmp_lg_u32 s67, 0
	s_cbranch_scc1 .Lpj_norm_1
	global_load_dwordx4 v[18:21], v[196:197], off offset:64
	global_load_dwordx4 v[22:25], v[196:197], off offset:128
	global_load_dwordx4 v[26:29], v[198:199], off
	global_load_dwordx4 v[30:33], v[198:199], off offset:64
	s_waitcnt vmcnt(16)
	s_branch .Lpj_join_1

.Lpj_join_1:
	s_barrier
	s_setprio 1
	s_waitcnt lgkmcnt(1)
	v_mfma_f32_16x16x32_f16 v[86:89], v[130:133], v[154:157], v[86:89]
	v_mfma_f32_16x16x32_f16 v[74:77], v[130:133], v[162:165], v[74:77]
	v_mfma_f32_16x16x32_f16 v[62:65], v[130:133], v[170:173], v[62:65]
	v_mfma_f32_16x16x32_f16 v[50:53], v[130:133], v[178:181], v[50:53]
	s_waitcnt lgkmcnt(0)
	v_mfma_f32_16x16x32_f16 v[86:89], v[142:145], v[158:161], v[86:89]
	v_mfma_f32_16x16x32_f16 v[74:77], v[142:145], v[166:169], v[74:77]
	v_mfma_f32_16x16x32_f16 v[62:65], v[142:145], v[174:177], v[62:65]
	v_mfma_f32_16x16x32_f16 v[50:53], v[142:145], v[182:185], v[50:53]
	s_setprio 0
	s_barrier
	s_mov_b32 m0, s56
	v_lshl_add_u64 v[108:109], v[108:109], 0, s[22:23]
	ds_read_b128 v[130:133], v138
	ds_read_b128 v[142:145], v138 offset:1024
	ds_read_b128 v[146:149], v138 offset:2048
	ds_read_b128 v[150:153], v138 offset:3072
	ds_read_b128 v[154:157], v139
	ds_read_b128 v[158:161], v139 offset:1024
	ds_read_b128 v[162:165], v139 offset:2048
	ds_read_b128 v[166:169], v139 offset:3072
	ds_read_b128 v[170:173], v139 offset:4096
	ds_read_b128 v[174:177], v139 offset:5120
	ds_read_b128 v[178:181], v139 offset:6144
	ds_read_b128 v[182:185], v139 offset:7168
	global_load_lds_dwordx4 v[108:109], off
	v_lshl_add_u64 v[108:109], v[186:187], 0, s[22:23]
	s_mov_b32 m0, s57
	s_nop 0
	global_load_lds_dwordx4 v[108:109], off
	s_barrier
	s_setprio 1
	s_waitcnt lgkmcnt(7)
	v_mfma_f32_16x16x32_f16 v[94:97], v[130:133], v[154:157], v[94:97]
	v_mfma_f32_16x16x32_f16 v[90:93], v[146:149], v[154:157], v[90:93]
	s_waitcnt lgkmcnt(5)
	v_mfma_f32_16x16x32_f16 v[82:85], v[130:133], v[162:165], v[82:85]
	v_mfma_f32_16x16x32_f16 v[78:81], v[146:149], v[162:165], v[78:81]
	s_waitcnt lgkmcnt(3)
	v_mfma_f32_16x16x32_f16 v[70:73], v[130:133], v[170:173], v[70:73]
	v_mfma_f32_16x16x32_f16 v[66:69], v[146:149], v[170:173], v[66:69]
	s_waitcnt lgkmcnt(1)
	v_mfma_f32_16x16x32_f16 v[58:61], v[130:133], v[178:181], v[58:61]
	v_mfma_f32_16x16x32_f16 v[54:57], v[146:149], v[178:181], v[54:57]
	v_mfma_f32_16x16x32_f16 v[94:97], v[142:145], v[158:161], v[94:97]
	v_mfma_f32_16x16x32_f16 v[90:93], v[150:153], v[158:161], v[90:93]
	v_mfma_f32_16x16x32_f16 v[82:85], v[142:145], v[166:169], v[82:85]
	v_mfma_f32_16x16x32_f16 v[78:81], v[150:153], v[166:169], v[78:81]
	v_mfma_f32_16x16x32_f16 v[70:73], v[142:145], v[174:177], v[70:73]
	v_mfma_f32_16x16x32_f16 v[66:69], v[150:153], v[174:177], v[66:69]
	s_waitcnt lgkmcnt(0)
	v_mfma_f32_16x16x32_f16 v[58:61], v[142:145], v[182:185], v[58:61]
	v_mfma_f32_16x16x32_f16 v[54:57], v[150:153], v[182:185], v[54:57]
	s_setprio 0
	s_barrier
	s_mov_b32 m0, s58
	v_lshl_add_u64 v[108:109], v[188:189], 0, s[22:23]
	ds_read_b128 v[130:133], v138 offset:4096
	ds_read_b128 v[142:145], v138 offset:5120
	global_load_lds_dwordx4 v[108:109], off
	v_lshl_add_u64 v[108:109], v[190:191], 0, s[22:23]
	s_add_i32 m0, s58, 0x2000
	s_nop 0
	global_load_lds_dwordx4 v[108:109], off
	v_lshl_add_u64 v[108:109], v[192:193], 0, s[22:23]
	s_add_i32 m0, s58, 0x4000
	s_nop 0
	global_load_lds_dwordx4 v[108:109], off
	s_cmp_lg_u32 s67, 0
	s_cbranch_scc1 .Lpj_norm_2
	global_load_dwordx4 v[34:37], v[198:199], off offset:128
	global_load_dwordx4 v[38:41], v[200:201], off
	global_load_dwordx4 v[42:45], v[200:201], off offset:64
	global_load_dwordx4 v[46:49], v[200:201], off offset:128
	s_waitcnt vmcnt(13)
	s_branch .Lpj_join_2

.Lpj_join_2:
	s_barrier
	s_setprio 1
	s_waitcnt lgkmcnt(1)
	v_mfma_f32_16x16x32_f16 v[86:89], v[130:133], v[154:157], v[86:89]
	v_mfma_f32_16x16x32_f16 v[74:77], v[130:133], v[162:165], v[74:77]
	v_mfma_f32_16x16x32_f16 v[62:65], v[130:133], v[170:173], v[62:65]
	v_mfma_f32_16x16x32_f16 v[50:53], v[130:133], v[178:181], v[50:53]
	s_waitcnt lgkmcnt(0)
	v_mfma_f32_16x16x32_f16 v[86:89], v[142:145], v[158:161], v[86:89]
	v_mfma_f32_16x16x32_f16 v[74:77], v[142:145], v[166:169], v[74:77]
	v_mfma_f32_16x16x32_f16 v[62:65], v[142:145], v[174:177], v[62:65]
	v_mfma_f32_16x16x32_f16 v[50:53], v[142:145], v[182:185], v[50:53]
	s_setprio 0
	s_barrier
	s_add_i32 s67, s67, 3
	s_add_u32 s30, s30, 0x180
	s_addc_u32 s31, s31, 0
	s_cmp_ge_i32 s67, s59
	s_cbranch_scc0 .LBB4_22

.LBB5_55:
	s_add_u32 s46, s40, s44
	s_addc_u32 s47, s41, s45
	s_add_u32 s46, s46, 0x180
	s_addc_u32 s47, s47, 0
	s_add_u32 s48, s42, s44
	s_addc_u32 s49, s43, s45
	s_add_u32 s76, s48, 0x180
	s_addc_u32 s77, s49, 0
	s_cmp_eq_u32 s67, s75
	s_cselect_b32 s49, s7, s47
	s_cselect_b32 s48, s6, s46
	s_cselect_b32 s47, s5, s77
	s_cselect_b32 s46, s4, s76
	s_add_i32 s76, s19, s54
	v_lshl_add_u64 v[126:127], v[32:33], 0, s[44:45]
	s_mov_b32 m0, s76
	ds_read_b128 v[44:47], v130 offset:16384
	ds_read_b128 v[56:59], v130 offset:17408
	ds_read_b128 v[60:63], v130 offset:18432
	ds_read_b128 v[64:67], v130 offset:19456
	ds_read_b128 v[68:71], v131
	ds_read_b128 v[96:99], v131 offset:1024
	ds_read_b128 v[136:139], v131 offset:2048
	ds_read_b128 v[140:143], v131 offset:3072
	ds_read_b128 v[144:147], v131 offset:4096
	ds_read_b128 v[148:151], v131 offset:5120
	ds_read_b128 v[152:155], v131 offset:6144
	ds_read_b128 v[156:159], v131 offset:7168
	global_load_lds_dwordx4 v[126:127], off
	v_lshl_add_u64 v[126:127], v[34:35], 0, s[44:45]
	s_add_i32 m0, s76, 0x2000
	s_add_i32 s76, s27, s54
	global_load_lds_dwordx4 v[126:127], off
	v_lshl_add_u64 v[126:127], v[36:37], 0, s[44:45]
	s_mov_b32 m0, s76
	s_nop 0
	global_load_lds_dwordx4 v[126:127], off
	v_lshl_add_u64 v[126:127], v[38:39], 0, s[44:45]
	s_add_i32 m0, s76, 0x2000
	s_nop 0
	global_load_lds_dwordx4 v[126:127], off
	s_barrier
	s_setprio 1
	s_waitcnt lgkmcnt(7)
	v_mfma_f32_16x16x32_f16 v[92:95], v[44:47], v[68:71], v[92:95]
	v_mfma_f32_16x16x32_f16 v[88:91], v[60:63], v[68:71], v[88:91]
	s_waitcnt lgkmcnt(5)
	v_mfma_f32_16x16x32_f16 v[76:79], v[44:47], v[136:139], v[76:79]
	v_mfma_f32_16x16x32_f16 v[72:75], v[60:63], v[136:139], v[72:75]
	s_waitcnt lgkmcnt(3)
	v_mfma_f32_16x16x32_f16 v[28:31], v[44:47], v[144:147], v[28:31]
	v_mfma_f32_16x16x32_f16 v[24:27], v[60:63], v[144:147], v[24:27]
	s_waitcnt lgkmcnt(1)
	v_mfma_f32_16x16x32_f16 v[12:15], v[44:47], v[152:155], v[12:15]
	v_mfma_f32_16x16x32_f16 v[8:11], v[60:63], v[152:155], v[8:11]
	v_mfma_f32_16x16x32_f16 v[92:95], v[56:59], v[96:99], v[92:95]
	v_mfma_f32_16x16x32_f16 v[88:91], v[64:67], v[96:99], v[88:91]
	v_mfma_f32_16x16x32_f16 v[76:79], v[56:59], v[140:143], v[76:79]
	v_mfma_f32_16x16x32_f16 v[72:75], v[64:67], v[140:143], v[72:75]
	v_mfma_f32_16x16x32_f16 v[28:31], v[56:59], v[148:151], v[28:31]
	v_mfma_f32_16x16x32_f16 v[24:27], v[64:67], v[148:151], v[24:27]
	s_waitcnt lgkmcnt(0)
	v_mfma_f32_16x16x32_f16 v[12:15], v[56:59], v[156:159], v[12:15]
	v_mfma_f32_16x16x32_f16 v[8:11], v[64:67], v[156:159], v[8:11]
	s_setprio 0
	s_barrier
	s_add_i32 s76, s68, s54
	v_lshl_add_u64 v[126:127], v[40:41], 0, s[44:45]
	s_mov_b32 m0, s76
	ds_read_b128 v[44:47], v130 offset:32768
	ds_read_b128 v[56:59], v130 offset:33792
	ds_read_b128 v[60:63], v130 offset:34816
	ds_read_b128 v[64:67], v130 offset:35840
	global_load_lds_dwordx4 v[126:127], off
	v_lshl_add_u64 v[126:127], v[42:43], 0, s[44:45]
	s_add_i32 m0, s76, 0x2000
	s_nop 0
	global_load_lds_dwordx4 v[126:127], off
	s_waitcnt vmcnt(6)
	s_barrier
	s_setprio 1
	s_waitcnt lgkmcnt(3)
	v_mfma_f32_16x16x32_f16 v[84:87], v[44:47], v[68:71], v[84:87]
	v_mfma_f32_16x16x32_f16 v[52:55], v[44:47], v[136:139], v[52:55]
	s_waitcnt lgkmcnt(1)
	v_mfma_f32_16x16x32_f16 v[48:51], v[60:63], v[136:139], v[48:51]
	v_mfma_f32_16x16x32_f16 v[20:23], v[44:47], v[144:147], v[20:23]
	v_mfma_f32_16x16x32_f16 v[16:19], v[60:63], v[144:147], v[16:19]
	v_mfma_f32_16x16x32_f16 v[4:7], v[44:47], v[152:155], v[4:7]
	v_mfma_f32_16x16x32_f16 v[0:3], v[60:63], v[152:155], v[0:3]
	v_mfma_f32_16x16x32_f16 v[84:87], v[56:59], v[96:99], v[84:87]
	v_mfma_f32_16x16x32_f16 v[68:71], v[60:63], v[68:71], v[80:83]
	v_mfma_f32_16x16x32_f16 v[52:55], v[56:59], v[140:143], v[52:55]
	s_waitcnt lgkmcnt(0)
	v_mfma_f32_16x16x32_f16 v[48:51], v[64:67], v[140:143], v[48:51]
	v_mfma_f32_16x16x32_f16 v[20:23], v[56:59], v[148:151], v[20:23]
	v_mfma_f32_16x16x32_f16 v[16:19], v[64:67], v[148:151], v[16:19]
	v_mfma_f32_16x16x32_f16 v[4:7], v[56:59], v[156:159], v[4:7]
	v_mfma_f32_16x16x32_f16 v[0:3], v[64:67], v[156:159], v[0:3]
	v_mfma_f32_16x16x32_f16 v[68:71], v[64:67], v[96:99], v[68:71]
	s_setprio 0
	s_barrier
	s_add_i32 s76, 0, 0x10000
	s_mov_b32 m0, s57
	v_add_u32_e32 v64, s76, v128
	v_lshl_add_u64 v[126:127], s[48:49], 0, v[100:101]
	ds_read_b128 v[44:47], v64
	ds_read_b128 v[56:59], v64 offset:1024
	ds_read_b128 v[60:63], v64 offset:2048
	ds_read_b128 v[64:67], v64 offset:3072
	ds_read_b128 v[80:83], v131 offset:49152
	ds_read_b128 v[96:99], v131 offset:50176
	ds_read_b128 v[136:139], v131 offset:51200
	ds_read_b128 v[140:143], v131 offset:52224
	ds_read_b128 v[144:147], v131 offset:53248
	ds_read_b128 v[148:151], v131 offset:54272
	ds_read_b128 v[152:155], v131 offset:55296
	ds_read_b128 v[156:159], v131 offset:56320
	global_load_lds_dwordx4 v[126:127], off
	v_lshl_add_u64 v[160:161], s[48:49], 0, v[104:105]
	s_mov_b32 m0, s58
	v_lshl_add_u64 v[162:163], s[46:47], 0, v[102:103]
	global_load_lds_dwordx4 v[160:161], off
	s_mov_b32 m0, s59
	v_lshl_add_u64 v[164:165], s[46:47], 0, v[106:107]
	global_load_lds_dwordx4 v[162:163], off
	s_mov_b32 m0, s60
	s_nop 0
	global_load_lds_dwordx4 v[164:165], off
	s_barrier
	s_setprio 1
	s_waitcnt lgkmcnt(7)
	v_mfma_f32_16x16x32_f16 v[92:95], v[44:47], v[80:83], v[92:95]
	v_mfma_f32_16x16x32_f16 v[88:91], v[60:63], v[80:83], v[88:91]
	s_waitcnt lgkmcnt(5)
	v_mfma_f32_16x16x32_f16 v[76:79], v[44:47], v[136:139], v[76:79]
	v_mfma_f32_16x16x32_f16 v[72:75], v[60:63], v[136:139], v[72:75]
	s_waitcnt lgkmcnt(3)
	v_mfma_f32_16x16x32_f16 v[28:31], v[44:47], v[144:147], v[28:31]
	v_mfma_f32_16x16x32_f16 v[24:27], v[60:63], v[144:147], v[24:27]
	s_waitcnt lgkmcnt(1)
	v_mfma_f32_16x16x32_f16 v[12:15], v[44:47], v[152:155], v[12:15]
	v_mfma_f32_16x16x32_f16 v[8:11], v[60:63], v[152:155], v[8:11]
	v_mfma_f32_16x16x32_f16 v[92:95], v[56:59], v[96:99], v[92:95]
	v_mfma_f32_16x16x32_f16 v[88:91], v[64:67], v[96:99], v[88:91]
	v_mfma_f32_16x16x32_f16 v[76:79], v[56:59], v[140:143], v[76:79]
	v_mfma_f32_16x16x32_f16 v[72:75], v[64:67], v[140:143], v[72:75]
	v_mfma_f32_16x16x32_f16 v[28:31], v[56:59], v[148:151], v[28:31]
	v_mfma_f32_16x16x32_f16 v[24:27], v[64:67], v[148:151], v[24:27]
	s_waitcnt lgkmcnt(0)
	v_mfma_f32_16x16x32_f16 v[12:15], v[56:59], v[156:159], v[12:15]
	v_mfma_f32_16x16x32_f16 v[8:11], v[64:67], v[156:159], v[8:11]
	s_setprio 0
	s_barrier
	s_add_i32 s48, 0, 0x14000
	s_add_u32 s46, s46, s10
	s_addc_u32 s47, s47, s11
	s_mov_b32 m0, s61
	v_add_u32_e32 v64, s48, v128
	v_lshl_add_u64 v[166:167], s[46:47], 0, v[102:103]
	ds_read_b128 v[44:47], v64
	ds_read_b128 v[56:59], v64 offset:1024
	ds_read_b128 v[60:63], v64 offset:2048
	ds_read_b128 v[64:67], v64 offset:3072
	global_load_lds_dwordx4 v[166:167], off
	v_lshl_add_u64 v[168:169], s[46:47], 0, v[106:107]
	s_mov_b32 m0, s62
	s_nop 0
	global_load_lds_dwordx4 v[168:169], off
	s_waitcnt vmcnt(6)
	s_barrier
	s_setprio 1
	s_waitcnt lgkmcnt(3)
	v_mfma_f32_16x16x32_f16 v[84:87], v[44:47], v[80:83], v[84:87]
	v_mfma_f32_16x16x32_f16 v[52:55], v[44:47], v[136:139], v[52:55]
	s_waitcnt lgkmcnt(1)
	v_mfma_f32_16x16x32_f16 v[48:51], v[60:63], v[136:139], v[48:51]
	v_mfma_f32_16x16x32_f16 v[20:23], v[44:47], v[144:147], v[20:23]
	v_mfma_f32_16x16x32_f16 v[16:19], v[60:63], v[144:147], v[16:19]
	v_mfma_f32_16x16x32_f16 v[4:7], v[44:47], v[152:155], v[4:7]
	v_mfma_f32_16x16x32_f16 v[0:3], v[60:63], v[152:155], v[0:3]
	v_mfma_f32_16x16x32_f16 v[84:87], v[56:59], v[96:99], v[84:87]
	v_mfma_f32_16x16x32_f16 v[68:71], v[60:63], v[80:83], v[68:71]
	v_mfma_f32_16x16x32_f16 v[52:55], v[56:59], v[140:143], v[52:55]
	s_waitcnt lgkmcnt(0)
	v_mfma_f32_16x16x32_f16 v[48:51], v[64:67], v[140:143], v[48:51]
	v_mfma_f32_16x16x32_f16 v[20:23], v[56:59], v[148:151], v[20:23]
	v_mfma_f32_16x16x32_f16 v[16:19], v[64:67], v[148:151], v[16:19]
	v_mfma_f32_16x16x32_f16 v[4:7], v[56:59], v[156:159], v[4:7]
	v_mfma_f32_16x16x32_f16 v[0:3], v[64:67], v[156:159], v[0:3]
	v_mfma_f32_16x16x32_f16 v[68:71], v[64:67], v[96:99], v[68:71]
	s_setprio 0
	s_barrier
	s_mov_b32 m0, s64
	v_lshl_add_u64 v[126:127], v[126:127], 0, s[22:23]
	ds_read_b128 v[44:47], v132
	ds_read_b128 v[56:59], v132 offset:1024
	ds_read_b128 v[60:63], v132 offset:2048
	ds_read_b128 v[64:67], v132 offset:3072
	ds_read_b128 v[80:83], v133
	ds_read_b128 v[96:99], v133 offset:1024
	ds_read_b128 v[136:139], v133 offset:2048
	ds_read_b128 v[140:143], v133 offset:3072
	ds_read_b128 v[144:147], v133 offset:4096
	ds_read_b128 v[148:151], v133 offset:5120
	ds_read_b128 v[152:155], v133 offset:6144
	ds_read_b128 v[156:159], v133 offset:7168
	global_load_lds_dwordx4 v[126:127], off
	v_lshl_add_u64 v[126:127], v[160:161], 0, s[22:23]
	s_mov_b32 m0, s65
	s_add_i32 s46, s76, s54
	global_load_lds_dwordx4 v[126:127], off
	v_lshl_add_u64 v[126:127], v[162:163], 0, s[22:23]
	s_mov_b32 m0, s46
	s_nop 0
	global_load_lds_dwordx4 v[126:127], off
	v_lshl_add_u64 v[126:127], v[164:165], 0, s[22:23]
	s_add_i32 m0, s46, 0x2000
	s_nop 0
	global_load_lds_dwordx4 v[126:127], off
	s_barrier
	s_setprio 1
	s_waitcnt lgkmcnt(7)
	v_mfma_f32_16x16x32_f16 v[92:95], v[44:47], v[80:83], v[92:95]
	v_mfma_f32_16x16x32_f16 v[88:91], v[60:63], v[80:83], v[88:91]
	s_waitcnt lgkmcnt(5)
	v_mfma_f32_16x16x32_f16 v[76:79], v[44:47], v[136:139], v[76:79]
	v_mfma_f32_16x16x32_f16 v[72:75], v[60:63], v[136:139], v[72:75]
	s_waitcnt lgkmcnt(3)
	v_mfma_f32_16x16x32_f16 v[28:31], v[44:47], v[144:147], v[28:31]
	v_mfma_f32_16x16x32_f16 v[24:27], v[60:63], v[144:147], v[24:27]
	s_waitcnt lgkmcnt(1)
	v_mfma_f32_16x16x32_f16 v[12:15], v[44:47], v[152:155], v[12:15]
	v_mfma_f32_16x16x32_f16 v[8:11], v[60:63], v[152:155], v[8:11]
	v_mfma_f32_16x16x32_f16 v[92:95], v[56:59], v[96:99], v[92:95]
	v_mfma_f32_16x16x32_f16 v[88:91], v[64:67], v[96:99], v[88:91]
	v_mfma_f32_16x16x32_f16 v[76:79], v[56:59], v[140:143], v[76:79]
	v_mfma_f32_16x16x32_f16 v[72:75], v[64:67], v[140:143], v[72:75]
	v_mfma_f32_16x16x32_f16 v[28:31], v[56:59], v[148:151], v[28:31]
	v_mfma_f32_16x16x32_f16 v[24:27], v[64:67], v[148:151], v[24:27]
	s_waitcnt lgkmcnt(0)
	v_mfma_f32_16x16x32_f16 v[12:15], v[56:59], v[156:159], v[12:15]
	v_mfma_f32_16x16x32_f16 v[8:11], v[64:67], v[156:159], v[8:11]
	s_setprio 0
	s_barrier
	s_add_i32 s46, s48, s54
	v_lshl_add_u64 v[126:127], v[166:167], 0, s[22:23]
	s_mov_b32 m0, s46
	ds_read_b128 v[44:47], v134
	ds_read_b128 v[56:59], v134 offset:1024
	ds_read_b128 v[60:63], v134 offset:2048
	ds_read_b128 v[64:67], v134 offset:3072
	global_load_lds_dwordx4 v[126:127], off
	v_lshl_add_u64 v[126:127], v[168:169], 0, s[22:23]
	s_add_i32 m0, s46, 0x2000
	s_nop 0
	global_load_lds_dwordx4 v[126:127], off
	s_waitcnt vmcnt(6)
	s_barrier
	s_setprio 1
	s_waitcnt lgkmcnt(3)
	v_mfma_f32_16x16x32_f16 v[84:87], v[44:47], v[80:83], v[84:87]
	s_waitcnt lgkmcnt(1)
	v_mfma_f32_16x16x32_f16 v[68:71], v[60:63], v[80:83], v[68:71]
	v_mfma_f32_16x16x32_f16 v[52:55], v[44:47], v[136:139], v[52:55]
	v_mfma_f32_16x16x32_f16 v[48:51], v[60:63], v[136:139], v[48:51]
	v_mfma_f32_16x16x32_f16 v[20:23], v[44:47], v[144:147], v[20:23]
	v_mfma_f32_16x16x32_f16 v[16:19], v[60:63], v[144:147], v[16:19]
	v_mfma_f32_16x16x32_f16 v[4:7], v[44:47], v[152:155], v[4:7]
	v_mfma_f32_16x16x32_f16 v[0:3], v[60:63], v[152:155], v[0:3]
	v_mfma_f32_16x16x32_f16 v[84:87], v[56:59], v[96:99], v[84:87]
	s_waitcnt lgkmcnt(0)
	v_mfma_f32_16x16x32_f16 v[80:83], v[64:67], v[96:99], v[68:71]
	v_mfma_f32_16x16x32_f16 v[52:55], v[56:59], v[140:143], v[52:55]
	v_mfma_f32_16x16x32_f16 v[48:51], v[64:67], v[140:143], v[48:51]
	v_mfma_f32_16x16x32_f16 v[20:23], v[56:59], v[148:151], v[20:23]
	v_mfma_f32_16x16x32_f16 v[16:19], v[64:67], v[148:151], v[16:19]
	v_mfma_f32_16x16x32_f16 v[4:7], v[56:59], v[156:159], v[4:7]
	v_mfma_f32_16x16x32_f16 v[0:3], v[64:67], v[156:159], v[0:3]
	s_setprio 0
	s_barrier
	s_add_i32 s75, s75, 3
	s_add_u32 s44, s44, 0x180
	s_addc_u32 s45, s45, 0
	s_cmp_ge_i32 s75, s66
	s_cbranch_scc0 .LBB5_55
	s_branch .LBB5_42

.LBB6_22:
	s_add_u32 s30, s22, s28
	s_addc_u32 s31, s23, s29
	s_add_u32 s30, s30, 0x180
	s_addc_u32 s31, s31, 0
	s_add_u32 s66, s24, s28
	s_addc_u32 s67, s25, s29
	s_add_u32 s68, s66, 0x180
	s_addc_u32 s69, s67, 0
	s_cmp_eq_u32 s60, s65
	s_cselect_b32 s67, s27, s31
	s_cselect_b32 s66, s26, s30
	s_cselect_b32 s31, s5, s69
	s_cselect_b32 s30, s4, s68
	s_add_i32 s68, s62, s42
	v_add_u32_e32 v131, 0, v128
	v_add_u32_e32 v182, 0, v127
	v_lshl_add_u64 v[180:181], v[116:117], 0, s[28:29]
	s_mov_b32 m0, s68
	ds_read_b128 v[132:135], v131 offset:16384
	ds_read_b128 v[136:139], v131 offset:17408
	ds_read_b128 v[140:143], v131 offset:18432
	ds_read_b128 v[144:147], v131 offset:19456
	ds_read_b128 v[148:151], v182
	ds_read_b128 v[152:155], v182 offset:1024
	ds_read_b128 v[156:159], v182 offset:2048
	ds_read_b128 v[160:163], v182 offset:3072
	ds_read_b128 v[164:167], v182 offset:4096
	ds_read_b128 v[168:171], v182 offset:5120
	ds_read_b128 v[172:175], v182 offset:6144
	ds_read_b128 v[176:179], v182 offset:7168
	global_load_lds_dwordx4 v[180:181], off
	v_lshl_add_u64 v[180:181], v[118:119], 0, s[28:29]
	s_add_i32 m0, s68, 0x2000
	s_nop 0
	global_load_lds_dwordx4 v[180:181], off
	s_barrier
	s_setprio 1
	s_waitcnt lgkmcnt(7)
	v_mfma_f32_16x16x32_f16 v[40:43], v[132:135], v[148:151], v[40:43]
	v_mfma_f32_16x16x32_f16 v[44:47], v[140:143], v[148:151], v[44:47]
	s_waitcnt lgkmcnt(5)
	v_mfma_f32_16x16x32_f16 v[32:35], v[132:135], v[156:159], v[32:35]
	v_mfma_f32_16x16x32_f16 v[28:31], v[140:143], v[156:159], v[28:31]
	s_waitcnt lgkmcnt(3)
	v_mfma_f32_16x16x32_f16 v[20:23], v[132:135], v[164:167], v[20:23]
	v_mfma_f32_16x16x32_f16 v[16:19], v[140:143], v[164:167], v[16:19]
	s_waitcnt lgkmcnt(1)
	v_mfma_f32_16x16x32_f16 v[8:11], v[132:135], v[172:175], v[8:11]
	v_mfma_f32_16x16x32_f16 v[4:7], v[140:143], v[172:175], v[4:7]
	v_mfma_f32_16x16x32_f16 v[40:43], v[136:139], v[152:155], v[40:43]
	v_mfma_f32_16x16x32_f16 v[44:47], v[144:147], v[152:155], v[44:47]
	v_mfma_f32_16x16x32_f16 v[32:35], v[136:139], v[160:163], v[32:35]
	v_mfma_f32_16x16x32_f16 v[28:31], v[144:147], v[160:163], v[28:31]
	v_mfma_f32_16x16x32_f16 v[20:23], v[136:139], v[168:171], v[20:23]
	v_mfma_f32_16x16x32_f16 v[16:19], v[144:147], v[168:171], v[16:19]
	s_waitcnt lgkmcnt(0)
	v_mfma_f32_16x16x32_f16 v[8:11], v[136:139], v[176:179], v[8:11]
	v_mfma_f32_16x16x32_f16 v[4:7], v[144:147], v[176:179], v[4:7]
	s_setprio 0
	s_barrier
	v_lshl_add_u64 v[140:141], v[120:121], 0, s[28:29]
	s_add_i32 m0, s47, 0x18000
	ds_read_b128 v[132:135], v131 offset:20480
	ds_read_b128 v[136:139], v131 offset:21504
	global_load_lds_dwordx4 v[140:141], off
	v_lshl_add_u64 v[140:141], v[122:123], 0, s[28:29]
	s_add_i32 m0, s47, 0x1a000
	s_nop 0
	global_load_lds_dwordx4 v[140:141], off
	v_lshl_add_u64 v[140:141], v[124:125], 0, s[28:29]
	s_add_i32 m0, s47, 0x1c000
	s_nop 0
	global_load_lds_dwordx4 v[140:141], off
	s_cmp_lg_u32 s65, 0
	s_cbranch_scc1 .Lm2_norm_0
	s_mul_i32 s70, s58, 0xc0
	v_add_u32_e32 v234, s70, v129
	v_ashrrev_i32_e32 v235, 31, v234
	v_lshlrev_b64 v[234:235], 2, v[234:235]
	v_lshl_add_u64 v[234:235], s[18:19], 0, v[234:235]
	global_load_dwordx4 v[222:225], v[234:235], off
	global_load_dwordx4 v[226:229], v[234:235], off offset:64
	global_load_dwordx4 v[230:233], v[234:235], off offset:128
	global_load_dwordx2 v[198:199], v[190:191], off
	global_load_dwordx2 v[200:201], v[190:191], off offset:32
	global_load_dwordx2 v[202:203], v[190:191], off offset:64
	global_load_dwordx2 v[204:205], v[192:193], off
	s_waitcnt vmcnt(12)
	s_branch .Lm2_join_0

.Lm2_join_0:
	s_barrier
	s_setprio 1
	s_waitcnt lgkmcnt(1)
	v_mfma_f32_16x16x32_f16 v[36:39], v[132:135], v[148:151], v[36:39]
	v_mfma_f32_16x16x32_f16 v[24:27], v[132:135], v[156:159], v[24:27]
	v_mfma_f32_16x16x32_f16 v[12:15], v[132:135], v[164:167], v[12:15]
	v_mfma_f32_16x16x32_f16 v[0:3], v[132:135], v[172:175], v[0:3]
	s_waitcnt lgkmcnt(0)
	v_mfma_f32_16x16x32_f16 v[36:39], v[136:139], v[152:155], v[36:39]
	v_mfma_f32_16x16x32_f16 v[24:27], v[136:139], v[160:163], v[24:27]
	v_mfma_f32_16x16x32_f16 v[12:15], v[136:139], v[168:171], v[12:15]
	v_mfma_f32_16x16x32_f16 v[0:3], v[136:139], v[176:179], v[0:3]
	s_setprio 0
	s_barrier
	s_mov_b32 m0, s47
	v_lshl_add_u64 v[180:181], s[66:67], 0, v[48:49]
	ds_read_b128 v[132:135], v131 offset:57344
	ds_read_b128 v[136:139], v131 offset:58368
	ds_read_b128 v[140:143], v131 offset:59392
	ds_read_b128 v[144:147], v131 offset:60416
	ds_read_b128 v[148:151], v182 offset:40960
	ds_read_b128 v[152:155], v182 offset:41984
	ds_read_b128 v[156:159], v182 offset:43008
	ds_read_b128 v[160:163], v182 offset:44032
	ds_read_b128 v[164:167], v182 offset:45056
	ds_read_b128 v[168:171], v182 offset:46080
	ds_read_b128 v[172:175], v182 offset:47104
	ds_read_b128 v[176:179], v182 offset:48128
	global_load_lds_dwordx4 v[180:181], off
	v_lshl_add_u64 v[182:183], s[66:67], 0, v[52:53]
	s_mov_b32 m0, s48
	s_nop 0
	global_load_lds_dwordx4 v[182:183], off
	s_barrier
	s_setprio 1
	s_waitcnt lgkmcnt(7)
	v_mfma_f32_16x16x32_f16 v[40:43], v[132:135], v[148:151], v[40:43]
	v_mfma_f32_16x16x32_f16 v[44:47], v[140:143], v[148:151], v[44:47]
	s_waitcnt lgkmcnt(5)
	v_mfma_f32_16x16x32_f16 v[32:35], v[132:135], v[156:159], v[32:35]
	v_mfma_f32_16x16x32_f16 v[28:31], v[140:143], v[156:159], v[28:31]
	s_waitcnt lgkmcnt(3)
	v_mfma_f32_16x16x32_f16 v[20:23], v[132:135], v[164:167], v[20:23]
	v_mfma_f32_16x16x32_f16 v[16:19], v[140:143], v[164:167], v[16:19]
	s_waitcnt lgkmcnt(1)
	v_mfma_f32_16x16x32_f16 v[8:11], v[132:135], v[172:175], v[8:11]
	v_mfma_f32_16x16x32_f16 v[4:7], v[140:143], v[172:175], v[4:7]
	v_mfma_f32_16x16x32_f16 v[40:43], v[136:139], v[152:155], v[40:43]
	v_mfma_f32_16x16x32_f16 v[44:47], v[144:147], v[152:155], v[44:47]
	v_mfma_f32_16x16x32_f16 v[32:35], v[136:139], v[160:163], v[32:35]
	v_mfma_f32_16x16x32_f16 v[28:31], v[144:147], v[160:163], v[28:31]
	v_mfma_f32_16x16x32_f16 v[20:23], v[136:139], v[168:171], v[20:23]
	v_mfma_f32_16x16x32_f16 v[16:19], v[144:147], v[168:171], v[16:19]
	s_waitcnt lgkmcnt(0)
	v_mfma_f32_16x16x32_f16 v[8:11], v[136:139], v[176:179], v[8:11]
	v_mfma_f32_16x16x32_f16 v[4:7], v[144:147], v[176:179], v[4:7]
	s_setprio 0
	s_barrier
	s_mov_b32 m0, s49
	v_lshl_add_u64 v[184:185], s[30:31], 0, v[50:51]
	ds_read_b128 v[132:135], v131 offset:61440
	ds_read_b128 v[136:139], v131 offset:62464
	global_load_lds_dwordx4 v[184:185], off
	v_lshl_add_u64 v[186:187], s[30:31], 0, v[54:55]
	s_mov_b32 m0, s50
	v_lshl_add_u64 v[188:189], s[30:31], 0, v[56:57]
	global_load_lds_dwordx4 v[186:187], off
	s_mov_b32 m0, s51
	s_nop 0
	global_load_lds_dwordx4 v[188:189], off
	s_cmp_lg_u32 s65, 0
	s_cbranch_scc1 .Lm2_norm_1
	global_load_dwordx2 v[206:207], v[192:193], off offset:32
	global_load_dwordx2 v[208:209], v[192:193], off offset:64
	global_load_dwordx2 v[210:211], v[194:195], off
	global_load_dwordx2 v[212:213], v[194:195], off offset:32
	s_waitcnt vmcnt(16)
	s_branch .Lm2_join_1

.Lm2_join_1:
	s_barrier
	s_setprio 1
	s_waitcnt lgkmcnt(1)
	v_mfma_f32_16x16x32_f16 v[36:39], v[132:135], v[148:151], v[36:39]
	v_mfma_f32_16x16x32_f16 v[24:27], v[132:135], v[156:159], v[24:27]
	v_mfma_f32_16x16x32_f16 v[12:15], v[132:135], v[164:167], v[12:15]
	v_mfma_f32_16x16x32_f16 v[0:3], v[132:135], v[172:175], v[0:3]
	s_waitcnt lgkmcnt(0)
	v_mfma_f32_16x16x32_f16 v[36:39], v[136:139], v[152:155], v[36:39]
	v_mfma_f32_16x16x32_f16 v[24:27], v[136:139], v[160:163], v[24:27]
	v_mfma_f32_16x16x32_f16 v[12:15], v[136:139], v[168:171], v[12:15]
	v_mfma_f32_16x16x32_f16 v[0:3], v[136:139], v[176:179], v[0:3]
	s_setprio 0
	s_barrier
	s_mov_b32 m0, s54
	v_add_u32_e32 v131, s62, v127
	v_lshl_add_u64 v[180:181], v[180:181], 0, s[20:21]
	ds_read_b128 v[132:135], v130
	ds_read_b128 v[136:139], v130 offset:1024
	ds_read_b128 v[140:143], v130 offset:2048
	ds_read_b128 v[144:147], v130 offset:3072
	ds_read_b128 v[148:151], v131
	ds_read_b128 v[152:155], v131 offset:1024
	ds_read_b128 v[156:159], v131 offset:2048
	ds_read_b128 v[160:163], v131 offset:3072
	ds_read_b128 v[164:167], v131 offset:4096
	ds_read_b128 v[168:171], v131 offset:5120
	ds_read_b128 v[172:175], v131 offset:6144
	ds_read_b128 v[176:179], v131 offset:7168
	global_load_lds_dwordx4 v[180:181], off
	v_lshl_add_u64 v[180:181], v[182:183], 0, s[20:21]
	s_mov_b32 m0, s55
	s_nop 0
	global_load_lds_dwordx4 v[180:181], off
	s_barrier
	s_setprio 1
	s_waitcnt lgkmcnt(7)
	v_mfma_f32_16x16x32_f16 v[40:43], v[132:135], v[148:151], v[40:43]
	v_mfma_f32_16x16x32_f16 v[44:47], v[140:143], v[148:151], v[44:47]
	s_waitcnt lgkmcnt(5)
	v_mfma_f32_16x16x32_f16 v[32:35], v[132:135], v[156:159], v[32:35]
	v_mfma_f32_16x16x32_f16 v[28:31], v[140:143], v[156:159], v[28:31]
	s_waitcnt lgkmcnt(3)
	v_mfma_f32_16x16x32_f16 v[20:23], v[132:135], v[164:167], v[20:23]
	v_mfma_f32_16x16x32_f16 v[16:19], v[140:143], v[164:167], v[16:19]
	s_waitcnt lgkmcnt(1)
	v_mfma_f32_16x16x32_f16 v[8:11], v[132:135], v[172:175], v[8:11]
	v_mfma_f32_16x16x32_f16 v[4:7], v[140:143], v[172:175], v[4:7]
	v_mfma_f32_16x16x32_f16 v[40:43], v[136:139], v[152:155], v[40:43]
	v_mfma_f32_16x16x32_f16 v[44:47], v[144:147], v[152:155], v[44:47]
	v_mfma_f32_16x16x32_f16 v[32:35], v[136:139], v[160:163], v[32:35]
	v_mfma_f32_16x16x32_f16 v[28:31], v[144:147], v[160:163], v[28:31]
	v_mfma_f32_16x16x32_f16 v[20:23], v[136:139], v[168:171], v[20:23]
	v_mfma_f32_16x16x32_f16 v[16:19], v[144:147], v[168:171], v[16:19]
	s_waitcnt lgkmcnt(0)
	v_mfma_f32_16x16x32_f16 v[8:11], v[136:139], v[176:179], v[8:11]
	v_mfma_f32_16x16x32_f16 v[4:7], v[144:147], v[176:179], v[4:7]
	s_setprio 0
	s_barrier
	s_mov_b32 m0, s56
	v_lshl_add_u64 v[140:141], v[184:185], 0, s[20:21]
	ds_read_b128 v[132:135], v130 offset:4096
	ds_read_b128 v[136:139], v130 offset:5120
	global_load_lds_dwordx4 v[140:141], off
	v_lshl_add_u64 v[140:141], v[186:187], 0, s[20:21]
	s_add_i32 m0, s56, 0x2000
	s_nop 0
	global_load_lds_dwordx4 v[140:141], off
	v_lshl_add_u64 v[140:141], v[188:189], 0, s[20:21]
	s_add_i32 m0, s56, 0x4000
	s_nop 0
	global_load_lds_dwordx4 v[140:141], off
	s_cmp_lg_u32 s65, 0
	s_cbranch_scc1 .Lm2_norm_2
	global_load_dwordx2 v[214:215], v[194:195], off offset:64
	global_load_dwordx2 v[216:217], v[196:197], off
	global_load_dwordx2 v[218:219], v[196:197], off offset:32
	global_load_dwordx2 v[220:221], v[196:197], off offset:64
	s_waitcnt vmcnt(13)
	s_branch .Lm2_join_2

.Lm2_join_2:
	s_barrier
	s_setprio 1
	s_waitcnt lgkmcnt(1)
	v_mfma_f32_16x16x32_f16 v[36:39], v[132:135], v[148:151], v[36:39]
	v_mfma_f32_16x16x32_f16 v[24:27], v[132:135], v[156:159], v[24:27]
	v_mfma_f32_16x16x32_f16 v[12:15], v[132:135], v[164:167], v[12:15]
	v_mfma_f32_16x16x32_f16 v[0:3], v[132:135], v[172:175], v[0:3]
	s_waitcnt lgkmcnt(0)
	v_mfma_f32_16x16x32_f16 v[36:39], v[136:139], v[152:155], v[36:39]
	v_mfma_f32_16x16x32_f16 v[24:27], v[136:139], v[160:163], v[24:27]
	v_mfma_f32_16x16x32_f16 v[12:15], v[136:139], v[168:171], v[12:15]
	v_mfma_f32_16x16x32_f16 v[0:3], v[136:139], v[176:179], v[0:3]
	s_setprio 0
	s_barrier
	s_add_i32 s65, s65, 3
	s_add_u32 s28, s28, 0x180
	s_addc_u32 s29, s29, 0
	s_cmp_ge_i32 s65, s59
	s_cbranch_scc0 .LBB6_22
	s_branch .LBB6_9
